# HGRN chunk-local loop: the entry vmcnt ladder (a full drain of the previous unit's stores for every unit but the first) is now taken only by the first unit
# baseline (speedup 1.0000x reference)
.LBB0_181:
	s_cmp_lg_u32 s56, s64
	s_cbranch_scc1 .Lhl_later
	s_waitcnt vmcnt(0)
.Lhl_later:
	s_add_i32 s67, s56, s52
	s_cmpk_gt_i32 s67, 0x5ff
	s_cselect_b64 s[48:49], -1, 0
	s_and_b64 vcc, exec, s[48:49]
	v_mov_b32_e32 v94, v32
	v_mov_b32_e32 v97, v42
	v_mov_b32_e32 v100, v47
	v_mov_b32_e32 v103, v141
	v_mov_b32_e32 v106, v143
	v_mov_b32_e32 v109, v145
	v_mov_b32_e32 v112, v147
	v_mov_b32_e32 v115, v150
	v_mov_b32_e32 v118, v151
	v_mov_b32_e32 v121, v152
	v_mov_b32_e32 v124, v155
	v_mov_b32_e32 v127, v157
	v_mov_b32_e32 v130, v159
	v_mov_b32_e32 v133, v161
	v_mov_b32_e32 v136, v163
	v_mov_b32_e32 v139, v166
	v_mov_b32_e32 v93, v43
	v_mov_b32_e32 v96, v46
	v_mov_b32_e32 v99, v140
	v_mov_b32_e32 v102, v142
	v_mov_b32_e32 v105, v144
	v_mov_b32_e32 v108, v146
	v_mov_b32_e32 v111, v148
	v_mov_b32_e32 v114, v149
	v_mov_b32_e32 v117, v153
	v_mov_b32_e32 v120, v154
	v_mov_b32_e32 v123, v156
	v_mov_b32_e32 v126, v158
	v_mov_b32_e32 v129, v160
	v_mov_b32_e32 v132, v162
	v_mov_b32_e32 v135, v164
	v_mov_b32_e32 v138, v165
	v_mov_b32_e32 v92, v6
	v_mov_b32_e32 v95, v7
	v_mov_b32_e32 v98, v10
	v_mov_b32_e32 v101, v11
	v_mov_b32_e32 v104, v14
	v_mov_b32_e32 v107, v15
	v_mov_b32_e32 v110, v18
	v_mov_b32_e32 v113, v19
	v_mov_b32_e32 v116, v22
	v_mov_b32_e32 v119, v23
	v_mov_b32_e32 v122, v34
	v_mov_b32_e32 v125, v35
	v_mov_b32_e32 v128, v38
	v_mov_b32_e32 v131, v39
	v_mov_b32_e32 v134, v33
	v_mov_b32_e32 v137, v45
	s_cbranch_vccnz .LBB0_183
	s_mul_hi_i32 s4, s67, 0x2aaaaaab
	s_lshr_b32 s5, s4, 31
	s_lshr_b32 s4, s4, 6
	s_add_i32 s4, s4, s5
	s_ashr_i32 s5, s67, 31
	s_lshr_b32 s5, s5, 26
	s_add_i32 s5, s67, s5
	s_ashr_i32 s5, s5, 6
	s_mul_hi_i32 s26, s5, 0x2aaaaaab
	s_lshr_b32 s27, s26, 31
	s_add_i32 s26, s26, s27
	s_mul_i32 s26, s26, 6
	s_sub_i32 s26, s5, s26
	s_lshl_b32 s4, s4, 12
	s_lshl_b32 s5, s5, 12
	s_sub_i32 s4, s4, s5
	s_add_i32 s4, s4, s66
	v_add_u32_e32 v8, s4, v82
	v_mov_b64_e32 v[4:5], s[28:29]
	v_mad_i64_i32 v[4:5], s[4:5], v8, s93, v[4:5]
	s_lshl_b32 s4, s26, 7
	s_ashr_i32 s5, s4, 31
	v_lshl_add_u64 v[4:5], s[4:5], 1, v[4:5]
	v_lshlrev_b32_e32 v8, 1, v26
	v_mov_b32_e32 v9, v1
	v_lshl_add_u64 v[4:5], v[4:5], 0, v[8:9]
	v_add_co_u32_e32 v8, vcc, s59, v4
	s_movk_i32 s4, 0x7000
	s_nop 0
	v_addc_co_u32_e32 v9, vcc, 0, v5, vcc
	global_load_ushort v92, v[8:9], off offset:2048 nt
	global_load_ushort v93, v[8:9], off offset:512 nt
	global_load_ushort v94, v[8:9], off offset:3584 nt
	v_add_co_u32_e32 v8, vcc, s4, v4
	s_mov_b32 s4, 0xd000
	s_nop 0
	v_addc_co_u32_e32 v9, vcc, 0, v5, vcc
	global_load_ushort v95, v[8:9], off offset:1536 nt
	global_load_ushort v96, v[8:9], off nt
	global_load_ushort v97, v[8:9], off offset:3072 nt
	v_add_co_u32_e32 v8, vcc, s4, v4
	s_mov_b32 s4, 0xc000
	s_nop 0
	v_addc_co_u32_e32 v9, vcc, 0, v5, vcc
	v_add_co_u32_e32 v12, vcc, s4, v4
	s_mov_b32 s4, 0x13000
	s_nop 0
	v_addc_co_u32_e32 v13, vcc, 0, v5, vcc
	global_load_ushort v98, v[8:9], off offset:1024 nt
	global_load_ushort v99, v[12:13], off offset:3584 nt
	global_load_ushort v100, v[8:9], off offset:2560 nt
	v_add_co_u32_e32 v8, vcc, s4, v4
	s_mov_b32 s4, 0x12000
	s_nop 0
	v_addc_co_u32_e32 v9, vcc, 0, v5, vcc
	v_add_co_u32_e32 v12, vcc, s4, v4
	s_mov_b32 s4, 0x19000
	s_nop 0
	v_addc_co_u32_e32 v13, vcc, 0, v5, vcc
	global_load_ushort v101, v[8:9], off offset:512 nt
	global_load_ushort v102, v[12:13], off offset:3072 nt
	global_load_ushort v103, v[8:9], off offset:2048 nt
	v_add_co_u32_e32 v8, vcc, s4, v4
	s_mov_b32 s4, 0x18000
	s_nop 0
	v_addc_co_u32_e32 v9, vcc, 0, v5, vcc
	v_add_co_u32_e32 v12, vcc, s4, v4
	s_mov_b32 s4, 0x1e000
	s_nop 0
	v_addc_co_u32_e32 v13, vcc, 0, v5, vcc
	global_load_ushort v104, v[8:9], off nt
	global_load_ushort v105, v[12:13], off offset:2560 nt
	global_load_ushort v106, v[8:9], off offset:1536 nt
	v_add_co_u32_e32 v8, vcc, s4, v4
	s_mov_b32 s4, 0x1f000
	s_nop 0
	v_addc_co_u32_e32 v9, vcc, 0, v5, vcc
	global_load_ushort v107, v[8:9], off offset:3584 nt
	global_load_ushort v108, v[8:9], off offset:2048 nt
	v_add_co_u32_e32 v8, vcc, s4, v4
	s_mov_b32 s4, 0x24000
	s_nop 0
	v_addc_co_u32_e32 v9, vcc, 0, v5, vcc
	global_load_ushort v109, v[8:9], off offset:1024 nt
	v_add_co_u32_e32 v8, vcc, s4, v4
	s_mov_b32 s4, 0x25000
	s_nop 0
	v_addc_co_u32_e32 v9, vcc, 0, v5, vcc
	global_load_ushort v110, v[8:9], off offset:3072 nt
	global_load_ushort v111, v[8:9], off offset:1536 nt
	v_add_co_u32_e32 v8, vcc, s4, v4
	s_mov_b32 s4, 0x2a000
	s_nop 0
	v_addc_co_u32_e32 v9, vcc, 0, v5, vcc
	global_load_ushort v112, v[8:9], off offset:512 nt
	v_add_co_u32_e32 v8, vcc, s4, v4
	s_mov_b32 s4, 0x2b000
	s_nop 0
	v_addc_co_u32_e32 v9, vcc, 0, v5, vcc
	global_load_ushort v113, v[8:9], off offset:2560 nt
	global_load_ushort v114, v[8:9], off offset:1024 nt
	v_add_co_u32_e32 v8, vcc, s4, v4
	s_mov_b32 s4, 0x30000
	s_nop 0
	v_addc_co_u32_e32 v9, vcc, 0, v5, vcc
	global_load_ushort v115, v[8:9], off nt
	v_add_co_u32_e32 v8, vcc, s4, v4
	s_mov_b32 s4, 0x36000
	s_nop 0
	v_addc_co_u32_e32 v9, vcc, 0, v5, vcc
	global_load_ushort v116, v[8:9], off offset:2048 nt
	global_load_ushort v117, v[8:9], off offset:512 nt
	global_load_ushort v118, v[8:9], off offset:3584 nt
	v_add_co_u32_e32 v8, vcc, s4, v4
	s_mov_b32 s4, 0x3c000
	s_nop 0
	v_addc_co_u32_e32 v9, vcc, 0, v5, vcc
	global_load_ushort v119, v[8:9], off offset:1536 nt
	global_load_ushort v120, v[8:9], off nt
	global_load_ushort v121, v[8:9], off offset:3072 nt
	v_add_co_u32_e32 v8, vcc, s4, v4
	s_mov_b32 s4, 0x3b000
	s_nop 0
	v_addc_co_u32_e32 v9, vcc, 0, v5, vcc
	v_add_co_u32_e32 v12, vcc, s4, v4
	s_mov_b32 s4, 0x42000
	s_nop 0
	v_addc_co_u32_e32 v13, vcc, 0, v5, vcc
	global_load_ushort v122, v[8:9], off offset:1024 nt
	global_load_ushort v123, v[12:13], off offset:3584 nt
	global_load_ushort v124, v[8:9], off offset:2560 nt
	v_add_co_u32_e32 v8, vcc, s4, v4
	s_mov_b32 s4, 0x41000
	s_nop 0
	v_addc_co_u32_e32 v9, vcc, 0, v5, vcc
	v_add_co_u32_e32 v12, vcc, s4, v4
	s_mov_b32 s4, 0x48000
	s_nop 0
	v_addc_co_u32_e32 v13, vcc, 0, v5, vcc
	global_load_ushort v125, v[8:9], off offset:512 nt
	global_load_ushort v126, v[12:13], off offset:3072 nt
	global_load_ushort v127, v[8:9], off offset:2048 nt
	v_add_co_u32_e32 v8, vcc, s4, v4
	s_mov_b32 s4, 0x47000
	s_nop 0
	v_addc_co_u32_e32 v9, vcc, 0, v5, vcc
	v_add_co_u32_e32 v12, vcc, s4, v4
	s_mov_b32 s4, 0x4d000
	s_nop 0
	v_addc_co_u32_e32 v13, vcc, 0, v5, vcc
	global_load_ushort v128, v[8:9], off nt
	global_load_ushort v129, v[12:13], off offset:2560 nt
	global_load_ushort v130, v[8:9], off offset:1536 nt
	v_add_co_u32_e32 v8, vcc, s4, v4
	s_mov_b32 s4, 0x4e000
	s_nop 0
	v_addc_co_u32_e32 v9, vcc, 0, v5, vcc
	global_load_ushort v131, v[8:9], off offset:3584 nt
	global_load_ushort v132, v[8:9], off offset:2048 nt
	v_add_co_u32_e32 v8, vcc, s4, v4
	s_mov_b32 s4, 0x53000
	s_nop 0
	v_addc_co_u32_e32 v9, vcc, 0, v5, vcc
	global_load_ushort v133, v[8:9], off offset:1024 nt
	v_add_co_u32_e32 v8, vcc, s4, v4
	s_nop 1
	v_addc_co_u32_e32 v9, vcc, 0, v5, vcc
	global_load_ushort v134, v[8:9], off offset:3072 nt
	global_load_ushort v135, v[8:9], off offset:1536 nt
	v_add_co_u32_e32 v8, vcc, 0x54000, v4
	s_nop 1
	v_addc_co_u32_e32 v9, vcc, 0, v5, vcc
	global_load_ushort v136, v[8:9], off offset:512 nt
	v_add_co_u32_e32 v8, vcc, 0x59000, v4
	s_nop 1
	v_addc_co_u32_e32 v9, vcc, 0, v5, vcc
	v_add_co_u32_e32 v4, vcc, 0x5a000, v4
	global_load_ushort v137, v[8:9], off offset:2560 nt
	global_load_ushort v138, v[8:9], off offset:1024 nt
	v_addc_co_u32_e32 v5, vcc, 0, v5, vcc
	global_load_ushort v139, v[4:5], off nt
